# phase 0: silu(c) prologue with all 16 loads in flight (was one dependent load per iteration), constant tile->job lookup; phase 7 router GEMM prefetch
# speedup vs baseline: 1.0090x; 1.0090x over previous
.LBB0_10:
.LBB0_11:
	s_load_dwordx2 s[4:5], s[0:1], 0x8
	v_lshlrev_b32_e32 v2, 2, v250
	v_add_u32_e32 v1, 0, v2
	v_add_u32_e32 v36, 0x1000, v2
	v_add_u32_e32 v37, 0x2000, v2
	v_add_u32_e32 v38, 0x3000, v2
	v_add_u32_e32 v39, 0x4000, v2
	v_add_u32_e32 v40, 0x5000, v2
	v_add_u32_e32 v41, 0x6000, v2
	v_add_u32_e32 v42, 0x7000, v2
	s_waitcnt lgkmcnt(0)
	global_load_dword v20, v2, s[4:5]
	global_load_dword v21, v2, s[4:5] offset:2048
	global_load_dword v22, v36, s[4:5]
	global_load_dword v23, v36, s[4:5] offset:2048
	global_load_dword v24, v37, s[4:5]
	global_load_dword v25, v37, s[4:5] offset:2048
	global_load_dword v26, v38, s[4:5]
	global_load_dword v27, v38, s[4:5] offset:2048
	global_load_dword v28, v39, s[4:5]
	global_load_dword v29, v39, s[4:5] offset:2048
	global_load_dword v30, v40, s[4:5]
	global_load_dword v31, v40, s[4:5] offset:2048
	global_load_dword v32, v41, s[4:5]
	global_load_dword v33, v41, s[4:5] offset:2048
	global_load_dword v34, v42, s[4:5]
	global_load_dword v35, v42, s[4:5] offset:2048
	s_waitcnt vmcnt(15)
	v_mul_f32_e32 v5, 0xbfb8aa3b, v20
	v_exp_f32_e32 v5, v5
	s_nop 0
	v_add_f32_e32 v5, 1.0, v5
	v_div_scale_f32 v6, s[10:11], v5, v5, v20
	v_rcp_f32_e32 v7, v6
	v_div_scale_f32 v8, vcc, v20, v5, v20
	v_fma_f32 v9, -v6, v7, 1.0
	v_fmac_f32_e32 v7, v9, v7
	v_mul_f32_e32 v9, v8, v7
	v_fma_f32 v10, -v6, v9, v8
	v_fmac_f32_e32 v9, v10, v7
	v_fma_f32 v6, -v6, v9, v8
	v_div_fmas_f32 v6, v6, v7, v9
	v_div_fixup_f32 v4, v6, v5, v20
	ds_write_b32 v1, v4 offset:0
	s_waitcnt vmcnt(14)
	v_mul_f32_e32 v5, 0xbfb8aa3b, v21
	v_exp_f32_e32 v5, v5
	s_nop 0
	v_add_f32_e32 v5, 1.0, v5
	v_div_scale_f32 v6, s[10:11], v5, v5, v21
	v_rcp_f32_e32 v7, v6
	v_div_scale_f32 v8, vcc, v21, v5, v21
	v_fma_f32 v9, -v6, v7, 1.0
	v_fmac_f32_e32 v7, v9, v7
	v_mul_f32_e32 v9, v8, v7
	v_fma_f32 v10, -v6, v9, v8
	v_fmac_f32_e32 v9, v10, v7
	v_fma_f32 v6, -v6, v9, v8
	v_div_fmas_f32 v6, v6, v7, v9
	v_div_fixup_f32 v4, v6, v5, v21
	ds_write_b32 v1, v4 offset:2048
	s_waitcnt vmcnt(13)
	v_mul_f32_e32 v5, 0xbfb8aa3b, v22
	v_exp_f32_e32 v5, v5
	s_nop 0
	v_add_f32_e32 v5, 1.0, v5
	v_div_scale_f32 v6, s[10:11], v5, v5, v22
	v_rcp_f32_e32 v7, v6
	v_div_scale_f32 v8, vcc, v22, v5, v22
	v_fma_f32 v9, -v6, v7, 1.0
	v_fmac_f32_e32 v7, v9, v7
	v_mul_f32_e32 v9, v8, v7
	v_fma_f32 v10, -v6, v9, v8
	v_fmac_f32_e32 v9, v10, v7
	v_fma_f32 v6, -v6, v9, v8
	v_div_fmas_f32 v6, v6, v7, v9
	v_div_fixup_f32 v4, v6, v5, v22
	ds_write_b32 v1, v4 offset:4096
	s_waitcnt vmcnt(12)
	v_mul_f32_e32 v5, 0xbfb8aa3b, v23
	v_exp_f32_e32 v5, v5
	s_nop 0
	v_add_f32_e32 v5, 1.0, v5
	v_div_scale_f32 v6, s[10:11], v5, v5, v23
	v_rcp_f32_e32 v7, v6
	v_div_scale_f32 v8, vcc, v23, v5, v23
	v_fma_f32 v9, -v6, v7, 1.0
	v_fmac_f32_e32 v7, v9, v7
	v_mul_f32_e32 v9, v8, v7
	v_fma_f32 v10, -v6, v9, v8
	v_fmac_f32_e32 v9, v10, v7
	v_fma_f32 v6, -v6, v9, v8
	v_div_fmas_f32 v6, v6, v7, v9
	v_div_fixup_f32 v4, v6, v5, v23
	ds_write_b32 v1, v4 offset:6144
	s_waitcnt vmcnt(11)
	v_mul_f32_e32 v5, 0xbfb8aa3b, v24
	v_exp_f32_e32 v5, v5
	s_nop 0
	v_add_f32_e32 v5, 1.0, v5
	v_div_scale_f32 v6, s[10:11], v5, v5, v24
	v_rcp_f32_e32 v7, v6
	v_div_scale_f32 v8, vcc, v24, v5, v24
	v_fma_f32 v9, -v6, v7, 1.0
	v_fmac_f32_e32 v7, v9, v7
	v_mul_f32_e32 v9, v8, v7
	v_fma_f32 v10, -v6, v9, v8
	v_fmac_f32_e32 v9, v10, v7
	v_fma_f32 v6, -v6, v9, v8
	v_div_fmas_f32 v6, v6, v7, v9
	v_div_fixup_f32 v4, v6, v5, v24
	ds_write_b32 v1, v4 offset:8192
	s_waitcnt vmcnt(10)
	v_mul_f32_e32 v5, 0xbfb8aa3b, v25
	v_exp_f32_e32 v5, v5
	s_nop 0
	v_add_f32_e32 v5, 1.0, v5
	v_div_scale_f32 v6, s[10:11], v5, v5, v25
	v_rcp_f32_e32 v7, v6
	v_div_scale_f32 v8, vcc, v25, v5, v25
	v_fma_f32 v9, -v6, v7, 1.0
	v_fmac_f32_e32 v7, v9, v7
	v_mul_f32_e32 v9, v8, v7
	v_fma_f32 v10, -v6, v9, v8
	v_fmac_f32_e32 v9, v10, v7
	v_fma_f32 v6, -v6, v9, v8
	v_div_fmas_f32 v6, v6, v7, v9
	v_div_fixup_f32 v4, v6, v5, v25
	ds_write_b32 v1, v4 offset:10240
	s_waitcnt vmcnt(9)
	v_mul_f32_e32 v5, 0xbfb8aa3b, v26
	v_exp_f32_e32 v5, v5
	s_nop 0
	v_add_f32_e32 v5, 1.0, v5
	v_div_scale_f32 v6, s[10:11], v5, v5, v26
	v_rcp_f32_e32 v7, v6
	v_div_scale_f32 v8, vcc, v26, v5, v26
	v_fma_f32 v9, -v6, v7, 1.0
	v_fmac_f32_e32 v7, v9, v7
	v_mul_f32_e32 v9, v8, v7
	v_fma_f32 v10, -v6, v9, v8
	v_fmac_f32_e32 v9, v10, v7
	v_fma_f32 v6, -v6, v9, v8
	v_div_fmas_f32 v6, v6, v7, v9
	v_div_fixup_f32 v4, v6, v5, v26
	ds_write_b32 v1, v4 offset:12288
	s_waitcnt vmcnt(8)
	v_mul_f32_e32 v5, 0xbfb8aa3b, v27
	v_exp_f32_e32 v5, v5
	s_nop 0
	v_add_f32_e32 v5, 1.0, v5
	v_div_scale_f32 v6, s[10:11], v5, v5, v27
	v_rcp_f32_e32 v7, v6
	v_div_scale_f32 v8, vcc, v27, v5, v27
	v_fma_f32 v9, -v6, v7, 1.0
	v_fmac_f32_e32 v7, v9, v7
	v_mul_f32_e32 v9, v8, v7
	v_fma_f32 v10, -v6, v9, v8
	v_fmac_f32_e32 v9, v10, v7
	v_fma_f32 v6, -v6, v9, v8
	v_div_fmas_f32 v6, v6, v7, v9
	v_div_fixup_f32 v4, v6, v5, v27
	ds_write_b32 v1, v4 offset:14336
	s_waitcnt vmcnt(7)
	v_mul_f32_e32 v5, 0xbfb8aa3b, v28
	v_exp_f32_e32 v5, v5
	s_nop 0
	v_add_f32_e32 v5, 1.0, v5
	v_div_scale_f32 v6, s[10:11], v5, v5, v28
	v_rcp_f32_e32 v7, v6
	v_div_scale_f32 v8, vcc, v28, v5, v28
	v_fma_f32 v9, -v6, v7, 1.0
	v_fmac_f32_e32 v7, v9, v7
	v_mul_f32_e32 v9, v8, v7
	v_fma_f32 v10, -v6, v9, v8
	v_fmac_f32_e32 v9, v10, v7
	v_fma_f32 v6, -v6, v9, v8
	v_div_fmas_f32 v6, v6, v7, v9
	v_div_fixup_f32 v4, v6, v5, v28
	ds_write_b32 v1, v4 offset:16384
	s_waitcnt vmcnt(6)
	v_mul_f32_e32 v5, 0xbfb8aa3b, v29
	v_exp_f32_e32 v5, v5
	s_nop 0
	v_add_f32_e32 v5, 1.0, v5
	v_div_scale_f32 v6, s[10:11], v5, v5, v29
	v_rcp_f32_e32 v7, v6
	v_div_scale_f32 v8, vcc, v29, v5, v29
	v_fma_f32 v9, -v6, v7, 1.0
	v_fmac_f32_e32 v7, v9, v7
	v_mul_f32_e32 v9, v8, v7
	v_fma_f32 v10, -v6, v9, v8
	v_fmac_f32_e32 v9, v10, v7
	v_fma_f32 v6, -v6, v9, v8
	v_div_fmas_f32 v6, v6, v7, v9
	v_div_fixup_f32 v4, v6, v5, v29
	ds_write_b32 v1, v4 offset:18432
	s_waitcnt vmcnt(5)
	v_mul_f32_e32 v5, 0xbfb8aa3b, v30
	v_exp_f32_e32 v5, v5
	s_nop 0
	v_add_f32_e32 v5, 1.0, v5
	v_div_scale_f32 v6, s[10:11], v5, v5, v30
	v_rcp_f32_e32 v7, v6
	v_div_scale_f32 v8, vcc, v30, v5, v30
	v_fma_f32 v9, -v6, v7, 1.0
	v_fmac_f32_e32 v7, v9, v7
	v_mul_f32_e32 v9, v8, v7
	v_fma_f32 v10, -v6, v9, v8
	v_fmac_f32_e32 v9, v10, v7
	v_fma_f32 v6, -v6, v9, v8
	v_div_fmas_f32 v6, v6, v7, v9
	v_div_fixup_f32 v4, v6, v5, v30
	ds_write_b32 v1, v4 offset:20480
	s_waitcnt vmcnt(4)
	v_mul_f32_e32 v5, 0xbfb8aa3b, v31
	v_exp_f32_e32 v5, v5
	s_nop 0
	v_add_f32_e32 v5, 1.0, v5
	v_div_scale_f32 v6, s[10:11], v5, v5, v31
	v_rcp_f32_e32 v7, v6
	v_div_scale_f32 v8, vcc, v31, v5, v31
	v_fma_f32 v9, -v6, v7, 1.0
	v_fmac_f32_e32 v7, v9, v7
	v_mul_f32_e32 v9, v8, v7
	v_fma_f32 v10, -v6, v9, v8
	v_fmac_f32_e32 v9, v10, v7
	v_fma_f32 v6, -v6, v9, v8
	v_div_fmas_f32 v6, v6, v7, v9
	v_div_fixup_f32 v4, v6, v5, v31
	ds_write_b32 v1, v4 offset:22528
	s_waitcnt vmcnt(3)
	v_mul_f32_e32 v5, 0xbfb8aa3b, v32
	v_exp_f32_e32 v5, v5
	s_nop 0
	v_add_f32_e32 v5, 1.0, v5
	v_div_scale_f32 v6, s[10:11], v5, v5, v32
	v_rcp_f32_e32 v7, v6
	v_div_scale_f32 v8, vcc, v32, v5, v32
	v_fma_f32 v9, -v6, v7, 1.0
	v_fmac_f32_e32 v7, v9, v7
	v_mul_f32_e32 v9, v8, v7
	v_fma_f32 v10, -v6, v9, v8
	v_fmac_f32_e32 v9, v10, v7
	v_fma_f32 v6, -v6, v9, v8
	v_div_fmas_f32 v6, v6, v7, v9
	v_div_fixup_f32 v4, v6, v5, v32
	ds_write_b32 v1, v4 offset:24576
	s_waitcnt vmcnt(2)
	v_mul_f32_e32 v5, 0xbfb8aa3b, v33
	v_exp_f32_e32 v5, v5
	s_nop 0
	v_add_f32_e32 v5, 1.0, v5
	v_div_scale_f32 v6, s[10:11], v5, v5, v33
	v_rcp_f32_e32 v7, v6
	v_div_scale_f32 v8, vcc, v33, v5, v33
	v_fma_f32 v9, -v6, v7, 1.0
	v_fmac_f32_e32 v7, v9, v7
	v_mul_f32_e32 v9, v8, v7
	v_fma_f32 v10, -v6, v9, v8
	v_fmac_f32_e32 v9, v10, v7
	v_fma_f32 v6, -v6, v9, v8
	v_div_fmas_f32 v6, v6, v7, v9
	v_div_fixup_f32 v4, v6, v5, v33
	ds_write_b32 v1, v4 offset:26624
	s_waitcnt vmcnt(1)
	v_mul_f32_e32 v5, 0xbfb8aa3b, v34
	v_exp_f32_e32 v5, v5
	s_nop 0
	v_add_f32_e32 v5, 1.0, v5
	v_div_scale_f32 v6, s[10:11], v5, v5, v34
	v_rcp_f32_e32 v7, v6
	v_div_scale_f32 v8, vcc, v34, v5, v34
	v_fma_f32 v9, -v6, v7, 1.0
	v_fmac_f32_e32 v7, v9, v7
	v_mul_f32_e32 v9, v8, v7
	v_fma_f32 v10, -v6, v9, v8
	v_fmac_f32_e32 v9, v10, v7
	v_fma_f32 v6, -v6, v9, v8
	v_div_fmas_f32 v6, v6, v7, v9
	v_div_fixup_f32 v4, v6, v5, v34
	ds_write_b32 v1, v4 offset:28672
	s_waitcnt vmcnt(0)
	v_mul_f32_e32 v5, 0xbfb8aa3b, v35
	v_exp_f32_e32 v5, v5
	s_nop 0
	v_add_f32_e32 v5, 1.0, v5
	v_div_scale_f32 v6, s[10:11], v5, v5, v35
	v_rcp_f32_e32 v7, v6
	v_div_scale_f32 v8, vcc, v35, v5, v35
	v_fma_f32 v9, -v6, v7, 1.0
	v_fmac_f32_e32 v7, v9, v7
	v_mul_f32_e32 v9, v8, v7
	v_fma_f32 v10, -v6, v9, v8
	v_fmac_f32_e32 v9, v10, v7
	v_fma_f32 v6, -v6, v9, v8
	v_div_fmas_f32 v6, v6, v7, v9
	v_div_fixup_f32 v4, v6, v5, v35
	ds_write_b32 v1, v4 offset:30720
	v_mbcnt_lo_u32_b32 v0, -1, 0
	v_lshrrev_b32_e32 v10, 6, v250
	v_and_b32_e32 v2, 15, v250
	v_bfe_u32 v11, v250, 4, 2
	v_mbcnt_hi_u32_b32 v1, -1, v0
	v_and_b32_e32 v3, 64, v1
	v_lshlrev_b32_e32 v13, 6, v2
	v_lshlrev_b32_e32 v6, 2, v2
	s_load_dwordx4 s[8:11], s[0:1], 0x10
	v_lshlrev_b32_e32 v14, 4, v2
	v_lshl_or_b32 v2, v10, 2, v11
	v_xor_b32_e32 v0, 16, v1
	v_add_u32_e32 v3, 64, v3
	v_mul_u32_u24_e32 v2, 0x3000, v2
	v_cmp_lt_i32_e32 vcc, v0, v3
	v_xor_b32_e32 v4, 32, v1
	v_and_b32_e32 v5, 0xf0, v250
	v_lshlrev_b32_e32 v8, 2, v2
	v_cndmask_b32_e32 v0, v1, v0, vcc
	v_cmp_lt_i32_e32 vcc, v4, v3
	v_bfe_u32 v3, v250, 2, 2
	v_lshlrev_b32_e32 v5, 2, v5
	v_add_u32_e32 v2, 0x480000, v8
	v_cndmask_b32_e32 v1, v1, v4, vcc
	v_and_b32_e32 v4, 3, v250
	v_add3_u32 v44, 0, v5, v6
	v_lshrrev_b32_e32 v5, 2, v250
	v_mul_u32_u24_e32 v46, 0x3000, v3
	v_mov_b32_e32 v3, 0
	v_or_b32_e32 v2, v2, v14
	v_and_or_b32 v45, v5, 60, v4
	s_waitcnt lgkmcnt(0)
	v_lshl_add_u64 v[4:5], s[8:9], 0, v[2:3]
	v_add_u32_e32 v2, 0x300000, v8
	v_or_b32_e32 v2, v2, v14
	v_lshl_add_u64 v[6:7], s[8:9], 0, v[2:3]
	v_add_u32_e32 v2, 0x180000, v8
	v_or_b32_e32 v2, v2, v14
	v_lshl_add_u64 v[8:9], s[8:9], 0, v[2:3]
	v_lshlrev_b32_e32 v2, 2, v11
	v_lshl_or_b32 v2, v10, 4, v2
	v_add_u32_e32 v47, 0, v2
	v_mul_u32_u24_e32 v2, 0x3000, v11
	s_mov_b32 s15, 0xc000
	v_mad_u32_u24 v2, v10, s15, v2
	v_lshl_add_u32 v12, v10, 10, 0
	s_movk_i32 s3, 0x100
	s_add_u32 s12, s76, 0x8000
	v_lshl_or_b32 v2, v2, 2, v14
	v_lshlrev_b32_e32 v0, 2, v0
	v_lshlrev_b32_e32 v1, 2, v1
	v_cmp_eq_u32_e32 vcc, 0, v11
	v_cmp_gt_u32_e64 s[4:5], s3, v250
	s_addc_u32 s13, s77, 0
	s_lshl_b32 s14, s2, 6
	s_lshl_b32 s3, s80, 6
	v_lshl_add_u64 v[10:11], s[8:9], 0, v[2:3]
	v_add_u32_e32 v2, v12, v13
	s_mov_b32 s16, s2
	s_barrier
	s_branch .LBB0_15
